# speedup vs baseline: 1.0165x; 1.0165x over previous
.LBB0_80:
	s_or_b64 exec, exec, s[2:3]
	v_add_u32_e32 v9, 32, v1
	v_cmp_gt_i32_e32 vcc, s6, v9
	v_mov_b32_e32 v3, 0
	v_mov_b32_e32 v5, 0
	s_and_saveexec_b64 s[2:3], vcc
	s_cbranch_execz .LBB0_82
	s_movk_i32 s1, 0xc00
	v_mad_i64_i32 v[12:13], s[10:11], v9, s1, v[6:7]
	global_load_dword v5, v[12:13], off nt
	s_sleep 2

.LBB0_90:
	s_or_b64 exec, exec, s[2:3]
	v_add_u32_e32 v13, 0x48, v1
	v_cmp_gt_i32_e32 vcc, s6, v13
	s_and_saveexec_b64 s[2:3], vcc
	s_cbranch_execz .LBB0_92
	s_movk_i32 s1, 0xc00
	v_mad_i64_i32 v[12:13], s[10:11], v13, s1, v[6:7]
	global_load_dword v12, v[12:13], off nt
	s_sleep 2

.LBB0_100:
	s_or_b64 exec, exec, s[2:3]
	v_add_u32_e32 v16, 0x70, v1
	v_cmp_gt_i32_e32 vcc, s6, v16
	v_mov_b32_e32 v22, 0
	v_mov_b32_e32 v23, 0
	s_and_saveexec_b64 s[2:3], vcc
	s_cbranch_execz .LBB0_102
	s_movk_i32 s1, 0xc00
	v_mad_i64_i32 v[16:17], s[10:11], v16, s1, v[6:7]
	global_load_dword v23, v[16:17], off nt
	s_sleep 2
